# strategy 8 (MFMA/LDS interleave) on top of v43: FoX attention compute issues all 8 K-fragment ds_reads up front with counted lgkmcnt waits, and P.V uses a 4-deep ring of transposed V fragments
# speedup vs baseline: 1.0057x; 1.0057x over previous
; #define LAS __attribute__((address_space(3)))
; template <int D, bool MASK, bool BIAS, bool SINK, bool REV, bool O8, class BG>
; __device__ __forceinline__ void attn_unit(const Prm& P, LAS unsigned char* lds, BG& bg) {
;     ...
;         if (MASK) {
;             compute = !(kbase > qw + 31 || kbase + 63 < qw - P.window + 1) && (!REV || need_cur != 0);
;             need_mask = (kbase + 63 > qw) || (kbase < qw + 31 - P.window + 1) || (kbase < 0);
;         }
;         if (compute) {
;             const float cinit = cq - mhat;
;             f32x16 p0, p1;
; #pragma unroll
;             for (int r = 0; r < 16; ++r) { p0[r] = cinit; p1[r] = cinit; }
;             const LAS unsigned char* ks = lds + KOFF + s * KSLOT + hi * 1024 + r32 * 16;
; #pragma unroll
;             for (int d0 = 0; d0 < NKS; ++d0) {
;                 const bf16x8 b0 = *(const LAS bf16x8*)(ks + d0 * 2048), b1 = *(const LAS bf16x8*)(ks + d0 * 2048 + 512);
;                 p0 = __builtin_amdgcn_mfma_f32_32x32x16_bf16(b0, qr[d0], p0, 0, 0, 0);
;                 p1 = __builtin_amdgcn_mfma_f32_32x32x16_bf16(b1, qr[d0], p1, 0, 0, 0);
;             }
;             if (BIAS) {
;                 const LAS float* cb = P.c + (kbase - P.cpos0) + 4 * hi;
; #pragma unroll
;                 for (int g = 0; g < 4; ++g) {
;                     const f32x4 a = *(const LAS f32x4*)(cb + 8 * g), b = *(const LAS f32x4*)(cb + 32 + 8 * g);
; #pragma unroll
;                     for (int j = 0; j < 4; ++j) { p0[4 * g + j] -= a[j]; p1[4 * g + j] -= b[j]; }
;                 }
.LBB0_466:
	s_cmp_le_i32 s58, s49
	s_cselect_b64 s[66:67], -1, 0
	s_or_b32 s6, s58, 63
	s_cmp_gt_i32 s6, s44
	s_cselect_b64 s[96:97], -1, 0
	v_cmp_ne_u32_e32 vcc, 0, v1
	s_and_b64 s[66:67], s[66:67], s[96:97]
	s_and_b64 s[66:67], s[66:67], vcc
	s_andn2_b64 vcc, exec, s[66:67]
	s_cbranch_vccnz .LBB0_478
	s_cmp_gt_i32 s6, s50
	s_cselect_b64 s[6:7], -1, 0
	s_cmp_lt_i32 s59, 0
	s_cselect_b64 s[66:67], -1, 0
	s_cmp_le_i32 s58, s51
	s_cselect_b64 s[96:97], -1, 0
	s_lshl_b32 s14, s57, 13
	v_add_u32_e32 v1, s14, v192
	ds_read_b128 v[36:39], v1
	ds_read_b128 v[40:43], v1 offset:512
	ds_read_b128 v[44:47], v1 offset:2048
	ds_read_b128 v[48:51], v1 offset:2560
	ds_read_b128 v[52:55], v1 offset:4096
	ds_read_b128 v[56:59], v1 offset:4608
	ds_read_b128 v[60:63], v1 offset:6144
	ds_read_b128 v[228:231], v1 offset:6656
	v_sub_f32_e32 v64, v221, v226
	v_mov_b32_e32 v65, v64
	v_mov_b32_e32 v66, v64
	v_mov_b32_e32 v67, v64
	v_mov_b32_e32 v68, v64
	v_mov_b32_e32 v69, v64
	v_mov_b32_e32 v70, v64
	v_mov_b32_e32 v71, v64
	v_mov_b32_e32 v72, v64
	v_mov_b32_e32 v73, v64
	v_mov_b32_e32 v74, v64
	v_mov_b32_e32 v75, v64
	v_mov_b32_e32 v76, v64
	v_mov_b32_e32 v77, v64
	v_mov_b32_e32 v78, v64
	v_mov_b32_e32 v79, v64
	s_or_b64 s[66:67], s[66:67], s[96:97]
	s_or_b64 s[6:7], s[6:7], s[66:67]
	s_waitcnt lgkmcnt(6)
	v_mfma_f32_32x32x16_bf16 v[80:95], v[36:39], v[160:163], v[64:79]
	s_andn2_b64 vcc, exec, s[6:7]
	v_mfma_f32_32x32x16_bf16 v[64:79], v[40:43], v[160:163], v[64:79]
	s_waitcnt lgkmcnt(4)
	v_mfma_f32_32x32x16_bf16 v[80:95], v[44:47], v[164:167], v[80:95]
	v_mfma_f32_32x32x16_bf16 v[64:79], v[48:51], v[164:167], v[64:79]
	s_waitcnt lgkmcnt(2)
	v_mfma_f32_32x32x16_bf16 v[80:95], v[52:55], v[168:171], v[80:95]
	v_mfma_f32_32x32x16_bf16 v[64:79], v[56:59], v[168:171], v[64:79]
	v_lshl_add_u32 v1, s58, 2, v196
	s_waitcnt lgkmcnt(0)
	v_mfma_f32_32x32x16_bf16 v[80:95], v[60:63], v[172:175], v[80:95]
	v_mfma_f32_32x32x16_bf16 v[64:79], v[228:231], v[172:175], v[64:79]
	ds_read_b128 v[228:231], v1 offset:128
	ds_read_b128 v[56:59], v1
	ds_read_b128 v[48:51], v1 offset:32
	ds_read_b128 v[60:63], v1 offset:160
	ds_read_b128 v[44:47], v1 offset:64
	ds_read_b128 v[232:235], v1 offset:192
	ds_read_b128 v[38:41], v1 offset:96
	ds_read_b128 v[236:239], v1 offset:224
	s_waitcnt lgkmcnt(0)
	s_nop 1
	v_sub_f32_e32 v51, v87, v51
	v_sub_f32_e32 v42, v90, v46
	v_sub_f32_e32 v46, v88, v44
	v_sub_f32_e32 v37, v95, v41
	v_sub_f32_e32 v36, v94, v40
	v_sub_f32_e32 v39, v93, v39
	v_sub_f32_e32 v38, v92, v38
	v_sub_f32_e32 v41, v91, v47
	v_sub_f32_e32 v47, v89, v45
	v_sub_f32_e32 v50, v86, v50
	v_sub_f32_e32 v55, v85, v49
	v_sub_f32_e32 v54, v84, v48
	v_sub_f32_e32 v59, v83, v59
	v_sub_f32_e32 v58, v82, v58
	v_sub_f32_e32 v1, v81, v57
	v_sub_f32_e32 v2, v80, v56
	v_sub_f32_e32 v43, v79, v239
	v_sub_f32_e32 v40, v78, v238
	v_sub_f32_e32 v45, v77, v237
	v_sub_f32_e32 v44, v76, v236
	v_sub_f32_e32 v49, v75, v235
	v_sub_f32_e32 v48, v74, v234
	v_sub_f32_e32 v53, v73, v233
	v_sub_f32_e32 v52, v72, v232
	v_sub_f32_e32 v57, v71, v63
	v_sub_f32_e32 v56, v70, v62
	v_sub_f32_e32 v61, v69, v61
	v_sub_f32_e32 v60, v68, v60
	v_sub_f32_e32 v63, v67, v231
	v_sub_f32_e32 v62, v66, v230
	v_sub_f32_e32 v65, v65, v229
	v_sub_f32_e32 v64, v64, v228
	s_cbranch_vccnz .LBB0_469
; template <int D, bool MASK, bool BIAS, bool SINK, bool REV, bool O8, class BG>
; __device__ __forceinline__ void attn_unit(const Prm& P, LAS unsigned char* lds, BG& bg) {
;     ...
;             if (MASK && need_mask) {
;                 const int dq = qpos - kbase; int lo = dq - P.window + 1; lo = lo > -kbase ? lo : -kbase;
;                 const int lo2 = lo - 4 * hi, hi2 = dq - 4 * hi;
; #pragma unroll
;                 for (int r = 0; r < 16; ++r) {
;                     const int kr = (r & 3) + 8 * (r >> 2);
;                     if (!(kr >= lo2 && kr <= hi2)) p0[r] = -INFINITY;
;                     if (!(kr + 32 >= lo2 && kr + 32 <= hi2)) p1[r] = -INFINITY;
;                 }
	v_subrev_u32_e32 v66, s58, v183
	v_add_u32_e32 v67, 0xc0000001, v66
	s_sub_i32 s6, 0, s58
	v_max_i32_e32 v67, s6, v67
	v_sub_u32_e32 v67, v67, v193
	v_sub_u32_e32 v66, v66, v193
	v_cmp_lt_i32_e32 vcc, 0, v67
	v_cmp_gt_i32_e64 s[6:7], 0, v66
	s_or_b64 vcc, vcc, s[6:7]
	v_cndmask_b32_e32 v2, v2, v216, vcc
	v_cmp_lt_i32_e32 vcc, 32, v67
	v_cmp_gt_i32_e64 s[6:7], 32, v66
	s_or_b64 vcc, vcc, s[6:7]
	v_cndmask_b32_e32 v64, v64, v216, vcc
	v_cmp_lt_i32_e32 vcc, 1, v67
	v_cmp_gt_i32_e64 s[6:7], 1, v66
	s_or_b64 vcc, vcc, s[6:7]
	v_cndmask_b32_e32 v1, v1, v216, vcc
	v_cmp_lt_i32_e32 vcc, 33, v67
	v_cmp_gt_i32_e64 s[6:7], 33, v66
	s_or_b64 vcc, vcc, s[6:7]
	v_cndmask_b32_e32 v65, v65, v216, vcc
	v_cmp_lt_i32_e32 vcc, 2, v67
	v_cmp_gt_i32_e64 s[6:7], 2, v66
	s_or_b64 vcc, vcc, s[6:7]
	v_cndmask_b32_e32 v58, v58, v216, vcc
	v_cmp_lt_i32_e32 vcc, 34, v67
	v_cmp_gt_i32_e64 s[6:7], 34, v66
	s_or_b64 vcc, vcc, s[6:7]
	v_cndmask_b32_e32 v62, v62, v216, vcc
	v_cmp_lt_i32_e32 vcc, 3, v67
	v_cmp_gt_i32_e64 s[6:7], 3, v66
	s_or_b64 vcc, vcc, s[6:7]
	v_cndmask_b32_e32 v59, v59, v216, vcc
	v_cmp_lt_i32_e32 vcc, 35, v67
	v_cmp_gt_i32_e64 s[6:7], 35, v66
	s_or_b64 vcc, vcc, s[6:7]
	v_cndmask_b32_e32 v63, v63, v216, vcc
	v_cmp_lt_i32_e32 vcc, 8, v67
	v_cmp_gt_i32_e64 s[6:7], 8, v66
	s_or_b64 vcc, vcc, s[6:7]
	v_cndmask_b32_e32 v54, v54, v216, vcc
	v_cmp_lt_i32_e32 vcc, 40, v67
	v_cmp_gt_i32_e64 s[6:7], 40, v66
	s_or_b64 vcc, vcc, s[6:7]
	v_cndmask_b32_e32 v60, v60, v216, vcc
	v_cmp_lt_i32_e32 vcc, 9, v67
	v_cmp_gt_i32_e64 s[6:7], 9, v66
	s_or_b64 vcc, vcc, s[6:7]
	v_cndmask_b32_e32 v55, v55, v216, vcc
	v_cmp_lt_i32_e32 vcc, 41, v67
	v_cmp_gt_i32_e64 s[6:7], 41, v66
	s_or_b64 vcc, vcc, s[6:7]
	v_cndmask_b32_e32 v61, v61, v216, vcc
	v_cmp_lt_i32_e32 vcc, 10, v67
	v_cmp_gt_i32_e64 s[6:7], 10, v66
	s_or_b64 vcc, vcc, s[6:7]
	v_cndmask_b32_e32 v50, v50, v216, vcc
	v_cmp_lt_i32_e32 vcc, 42, v67
	v_cmp_gt_i32_e64 s[6:7], 42, v66
	s_or_b64 vcc, vcc, s[6:7]
	v_cndmask_b32_e32 v56, v56, v216, vcc
	v_cmp_lt_i32_e32 vcc, 11, v67
	v_cmp_gt_i32_e64 s[6:7], 11, v66
	s_or_b64 vcc, vcc, s[6:7]
	v_cndmask_b32_e32 v51, v51, v216, vcc
	v_cmp_lt_i32_e32 vcc, 43, v67
	v_cmp_gt_i32_e64 s[6:7], 43, v66
	s_or_b64 vcc, vcc, s[6:7]
	v_cndmask_b32_e32 v57, v57, v216, vcc
	v_cmp_lt_i32_e32 vcc, 16, v67
	v_cmp_gt_i32_e64 s[6:7], 16, v66
	s_or_b64 vcc, vcc, s[6:7]
	v_cndmask_b32_e32 v46, v46, v216, vcc
	v_cmp_lt_i32_e32 vcc, 48, v67
	v_cmp_gt_i32_e64 s[6:7], 48, v66
	s_or_b64 vcc, vcc, s[6:7]
	v_cndmask_b32_e32 v52, v52, v216, vcc
	v_cmp_lt_i32_e32 vcc, 17, v67
	v_cmp_gt_i32_e64 s[6:7], 17, v66
	s_or_b64 vcc, vcc, s[6:7]
	v_cndmask_b32_e32 v47, v47, v216, vcc
	v_cmp_lt_i32_e32 vcc, 49, v67
	v_cmp_gt_i32_e64 s[6:7], 49, v66
	s_or_b64 vcc, vcc, s[6:7]
	v_cndmask_b32_e32 v53, v53, v216, vcc
	v_cmp_lt_i32_e32 vcc, 18, v67
	v_cmp_gt_i32_e64 s[6:7], 18, v66
	s_or_b64 vcc, vcc, s[6:7]
	v_cndmask_b32_e32 v42, v42, v216, vcc
	v_cmp_lt_i32_e32 vcc, 50, v67
	v_cmp_gt_i32_e64 s[6:7], 50, v66
	s_or_b64 vcc, vcc, s[6:7]
	v_cndmask_b32_e32 v48, v48, v216, vcc
	v_cmp_lt_i32_e32 vcc, 19, v67
	v_cmp_gt_i32_e64 s[6:7], 19, v66
	s_or_b64 vcc, vcc, s[6:7]
	v_cndmask_b32_e32 v41, v41, v216, vcc
	v_cmp_lt_i32_e32 vcc, 51, v67
	v_cmp_gt_i32_e64 s[6:7], 51, v66
	s_or_b64 vcc, vcc, s[6:7]
	v_cndmask_b32_e32 v49, v49, v216, vcc
	v_cmp_lt_i32_e32 vcc, 24, v67
	v_cmp_gt_i32_e64 s[6:7], 24, v66
	s_or_b64 vcc, vcc, s[6:7]
	v_cndmask_b32_e32 v38, v38, v216, vcc
	v_cmp_lt_i32_e32 vcc, 56, v67
	v_cmp_gt_i32_e64 s[6:7], 56, v66
	s_or_b64 vcc, vcc, s[6:7]
	v_cndmask_b32_e32 v44, v44, v216, vcc
	v_cmp_lt_i32_e32 vcc, 25, v67
	v_cmp_gt_i32_e64 s[6:7], 25, v66
	s_or_b64 vcc, vcc, s[6:7]
	v_cndmask_b32_e32 v39, v39, v216, vcc
	v_cmp_lt_i32_e32 vcc, 57, v67
	v_cmp_gt_i32_e64 s[6:7], 57, v66
	s_or_b64 vcc, vcc, s[6:7]
	v_cndmask_b32_e32 v45, v45, v216, vcc
	v_cmp_lt_i32_e32 vcc, 26, v67
	v_cmp_gt_i32_e64 s[6:7], 26, v66
	s_or_b64 vcc, vcc, s[6:7]
	v_cndmask_b32_e32 v36, v36, v216, vcc
	v_cmp_lt_i32_e32 vcc, 58, v67
	v_cmp_gt_i32_e64 s[6:7], 58, v66
	s_or_b64 vcc, vcc, s[6:7]
	v_cndmask_b32_e32 v40, v40, v216, vcc
	v_cmp_lt_i32_e32 vcc, 27, v67
	v_cmp_gt_i32_e64 s[6:7], 27, v66
	s_or_b64 vcc, vcc, s[6:7]
	v_cndmask_b32_e32 v37, v37, v216, vcc
	v_cmp_lt_i32_e32 vcc, 59, v67
	v_cmp_gt_i32_e64 s[6:7], 59, v66
	s_or_b64 vcc, vcc, s[6:7]
	v_cndmask_b32_e32 v43, v43, v216, vcc

; #define LAS __attribute__((address_space(3)))
; __device__ __forceinline__ unsigned cvtpk(float lo, float hi) { typedef __bf16 bf16x2_t __attribute__((ext_vector_type(2))); f32x2 v = {lo, hi}; bf16x2_t b = __builtin_convertvector(v, bf16x2_t); return __builtin_bit_cast(unsigned, b); }
; __device__ __forceinline__ s16x4 vtr(const LAS unsigned char* p) { return __builtin_bit_cast(s16x4, __builtin_amdgcn_ds_read_tr16_b64_v4i16((LAS v4i16_t*)p)); }
; template <int D, bool MASK, bool BIAS, bool SINK, bool REV, bool O8, class BG>
; __device__ __forceinline__ void attn_unit(const Prm& P, LAS unsigned char* lds, BG& bg) {
;     ...
;             float sacc = 0.f;
; #pragma unroll
;             for (int r = 0; r < 16; ++r) { p0[r] = __builtin_amdgcn_exp2f(p0[r]); p1[r] = __builtin_amdgcn_exp2f(p1[r]); sacc += p0[r] + p1[r]; }
;             l_reg += sacc;
;             u32x4 pw[4];
; #pragma unroll
;             for (int q = 0; q < 4; ++q) { pw[0][q] = cvtpk(p0[2 * q], p0[2 * q + 1]); pw[1][q] = cvtpk(p0[8 + 2 * q], p0[9 + 2 * q]); pw[2][q] = cvtpk(p1[2 * q], p1[2 * q + 1]); pw[3][q] = cvtpk(p1[8 + 2 * q], p1[9 + 2 * q]); }
;             const LAS unsigned char* vs = lds + VOFF + s * KSLOT + ((lane >> 4) & 1) * 32 + (lane & 3) * 8 + (4 * hi + ((lane & 15) >> 2)) * 64;
; #pragma unroll
;             for (int d = 0; d < NDB; ++d)
; #pragma unroll
;                 for (int k4 = 0; k4 < 4; ++k4) {
;                     const s16x4 vlo = vtr(vs + d * 4096 + k4 * 1024), vhi = vtr(vs + d * 4096 + k4 * 1024 + 512);
;                     const bf16x8 vf = (bf16x8){vlo[0], vlo[1], vlo[2], vlo[3], vhi[0], vhi[1], vhi[2], vhi[3]};
;                     o[d] = __builtin_amdgcn_mfma_f32_32x32x16_bf16(__builtin_bit_cast(bf16x8, pw[k4]), vf, o[d], 0, 0, 0);
;                 }
.LBB0_477:
	v_exp_f32_e32 v78, v2
	v_exp_f32_e32 v79, v64
	v_exp_f32_e32 v2, v1
	v_exp_f32_e32 v66, v65
	v_exp_f32_e32 v1, v58
	v_add_f32_e32 v67, v79, v78
	v_exp_f32_e32 v68, v63
	v_pk_add_f32 v[64:65], v[66:67], v[2:3]
	v_exp_f32_e32 v67, v62
	v_pk_add_f32 v[64:65], v[64:65], v[64:65] op_sel_hi:[0,1]
	v_exp_f32_e32 v64, v59
	v_exp_f32_e32 v62, v61
	v_add_f32_e32 v69, v67, v1
	v_exp_f32_e32 v42, v42
	v_pk_add_f32 v[58:59], v[68:69], v[64:65]
	v_exp_f32_e32 v65, v54
	v_pk_add_f32 v[58:59], v[58:59], v[58:59] op_sel_hi:[0,1]
	v_exp_f32_e32 v69, v60
	v_exp_f32_e32 v58, v55
	v_exp_f32_e32 v60, v57
	v_exp_f32_e32 v72, v45
	v_add_f32_e32 v63, v69, v65
	v_pk_add_f32 v[54:55], v[62:63], v[58:59]
	v_exp_f32_e32 v59, v50
	v_pk_add_f32 v[54:55], v[54:55], v[54:55] op_sel_hi:[0,1]
	v_exp_f32_e32 v63, v56
	v_exp_f32_e32 v54, v51
	v_exp_f32_e32 v56, v53
	v_exp_f32_e32 v76, v43
	v_add_f32_e32 v61, v63, v59
	v_pk_add_f32 v[50:51], v[60:61], v[54:55]
	v_exp_f32_e32 v55, v46
	v_pk_add_f32 v[50:51], v[50:51], v[50:51] op_sel_hi:[0,1]
	v_exp_f32_e32 v61, v52
	v_exp_f32_e32 v50, v47
	v_exp_f32_e32 v52, v49
	v_cvt_pk_bf16_f32 v43, v59, v54
	v_add_f32_e32 v57, v61, v55
	v_pk_add_f32 v[46:47], v[56:57], v[50:51]
	v_exp_f32_e32 v51, v48
	v_pk_add_f32 v[46:47], v[46:47], v[46:47] op_sel_hi:[0,1]
	v_exp_f32_e32 v46, v41
	v_exp_f32_e32 v57, v40
	v_add_f32_e32 v53, v51, v42
	v_cvt_pk_bf16_f32 v41, v1, v64
	v_pk_add_f32 v[48:49], v[52:53], v[46:47]
	v_exp_f32_e32 v47, v38
	v_pk_add_f32 v[70:71], v[48:49], v[48:49] op_sel_hi:[0,1]
	v_exp_f32_e32 v53, v44
	v_exp_f32_e32 v70, v39
	v_add_u32_e32 v1, s14, v194
	v_cvt_pk_bf16_f32 v40, v78, v2
	v_add_f32_e32 v73, v53, v47
	v_pk_add_f32 v[38:39], v[72:73], v[70:71]
	v_cvt_pk_bf16_f32 v44, v55, v50
	v_pk_add_f32 v[74:75], v[38:39], v[38:39] op_sel_hi:[0,1]
	v_exp_f32_e32 v39, v36
	v_exp_f32_e32 v74, v37
	v_cvt_pk_bf16_f32 v45, v42, v46
	v_cvt_pk_bf16_f32 v42, v65, v58
	v_add_f32_e32 v77, v57, v39
	v_pk_add_f32 v[36:37], v[76:77], v[74:75]
	v_cvt_pk_bf16_f32 v38, v53, v72
	v_add_f32_e32 v71, v36, v37
	v_cvt_pk_bf16_f32 v37, v51, v52
	s_nop 0
	ds_read_b64_tr_b16 v[52:53], v1 offset:32768
	ds_read_b64_tr_b16 v[54:55], v1 offset:33280
	ds_read_b64_tr_b16 v[240:241], v1 offset:33792
	ds_read_b64_tr_b16 v[242:243], v1 offset:34304
	ds_read_b64_tr_b16 v[244:245], v1 offset:34816
	ds_read_b64_tr_b16 v[246:247], v1 offset:35328
	ds_read_b64_tr_b16 v[248:249], v1 offset:35840
	ds_read_b64_tr_b16 v[250:251], v1 offset:36352
	v_cvt_pk_bf16_f32 v46, v47, v70
	v_cvt_pk_bf16_f32 v47, v39, v74
	s_waitcnt lgkmcnt(6)
	v_mfma_f32_32x32x16_bf16 v[4:19], v[40:43], v[52:55], v[4:19]
	ds_read_b64_tr_b16 v[52:53], v1 offset:36864
	ds_read_b64_tr_b16 v[54:55], v1 offset:37376
	v_cvt_pk_bf16_f32 v48, v79, v66
	v_cvt_pk_bf16_f32 v49, v67, v68
	v_cvt_pk_bf16_f32 v50, v69, v62
	v_cvt_pk_bf16_f32 v51, v63, v60
	s_waitcnt lgkmcnt(6)
	v_mfma_f32_32x32x16_bf16 v[4:19], v[44:47], v[240:243], v[4:19]
	ds_read_b64_tr_b16 v[240:241], v1 offset:37888
	ds_read_b64_tr_b16 v[242:243], v1 offset:38400
	v_cvt_pk_bf16_f32 v36, v61, v56
	v_cvt_pk_bf16_f32 v39, v57, v76
	v_add_f32_e32 v225, v225, v71
	s_mov_b64 s[92:93], 0
	s_waitcnt lgkmcnt(6)
	v_mfma_f32_32x32x16_bf16 v[4:19], v[48:51], v[244:247], v[4:19]
	ds_read_b64_tr_b16 v[244:245], v1 offset:38912
	ds_read_b64_tr_b16 v[246:247], v1 offset:39424
	s_waitcnt lgkmcnt(6)
	v_mfma_f32_32x32x16_bf16 v[4:19], v[36:39], v[248:251], v[4:19]
	ds_read_b64_tr_b16 v[248:249], v1 offset:39936
	ds_read_b64_tr_b16 v[250:251], v1 offset:40448
	s_waitcnt lgkmcnt(6)
	v_mfma_f32_32x32x16_bf16 v[20:35], v[40:43], v[52:55], v[20:35]
	s_waitcnt lgkmcnt(4)
	v_mfma_f32_32x32x16_bf16 v[20:35], v[44:47], v[240:243], v[20:35]
	s_waitcnt lgkmcnt(2)
	v_mfma_f32_32x32x16_bf16 v[20:35], v[48:51], v[244:247], v[20:35]
	s_waitcnt lgkmcnt(0)
	v_mfma_f32_32x32x16_bf16 v[20:35], v[36:39], v[248:251], v[20:35]
